# stack F plus: diff-attention unit prologue issues the bias scalar load and the distance-table load together and waits once
# baseline (speedup 1.0000x reference)
.LBB0_632:
	s_lshl_b32 s0, s40, 1
	s_lshr_b32 s5, s9, 6
	s_add_i32 s5, s5, s0
	s_and_b32 s4, s5, 7
	s_lshl_b32 s0, s4, 2
	v_readlane_b32 s12, v254, 12
	v_mov_b32_e32 v1, s0
	v_readlane_b32 s22, v254, 22
	v_readlane_b32 s23, v254, 23
	v_readfirstlane_b32 s2, v0
	v_readlane_b32 s13, v254, 13
	v_readlane_b32 s14, v254, 14
	v_readlane_b32 s15, v254, 15
	v_readlane_b32 s16, v254, 16
	global_load_dword v1, v1, s[22:23] offset:992
	v_readlane_b32 s17, v254, 17
	v_readlane_b32 s18, v254, 18
	v_readlane_b32 s19, v254, 19
	v_readlane_b32 s20, v254, 20
	v_readlane_b32 s21, v254, 21
	v_readlane_b32 s24, v254, 24
	v_readlane_b32 s25, v254, 25
	v_readlane_b32 s26, v254, 26
	v_readlane_b32 s27, v254, 27
	s_mov_b64 s[0:1], exec
	v_readlane_b32 s10, v255, 1
	v_readlane_b32 s11, v255, 2
	s_and_b64 s[10:11], s[0:1], s[10:11]
	s_mov_b64 exec, s[10:11]
	s_cbranch_execz .Lpro_nold
	v_or_b32_e32 v2, s4, v215
	v_lshl_add_u64 v[4:5], v[2:3], 2, s[22:23]
	global_load_dword v100, v[4:5], off
.Lpro_nold:
	s_mov_b64 exec, s[0:1]
	s_barrier
	s_waitcnt vmcnt(0)
	v_mul_f32_e32 v68, 0x3fb8aa3b, v1
	s_mov_b64 exec, s[10:11]
	s_cbranch_execz .LBB0_634
	v_fma_f32 v1, v100, s80, -v68
	ds_write_b32 v217, v1
